# baseline (speedup 1.0000x reference)
.Lskip_stage0:
	s_ashr_i32 s2, s4, 6
	s_lshl_b32 s3, s2, 3
	s_and_b32 s5, s3, 8
	s_bfe_u32 s26, s2, 0x10001
	s_or_b32 s5, s26, s5
	s_lshl_b32 s26, s2, 9
	s_and_b32 s26, s26, 0x400
	s_lshl_b32 s5, s5, 4
	s_or_b32 s28, s5, s26
	v_lshrrev_b32_e32 v182, 5, v167
	v_bfe_u32 v2, v156, 4, 1
	v_bitop3_b32 v3, v182, v156, 1 bitop3:0x78
	v_lshlrev_b32_e32 v154, 2, v182
	v_xor_b32_e32 v3, v3, v2
	v_bitop3_b32 v4, v154, v156, 4 bitop3:0x78
	v_and_b32_e32 v5, 10, v156
	v_or3_b32 v3, v5, v4, v3
	s_lshl_b32 s5, s2, 4
	v_lshlrev_b32_e32 v3, 4, v3
	s_lshl_b32 s3, s2, 13
	s_and_b32 s29, s5, 16
	v_lshlrev_b32_e32 v170, 8, v182
	v_lshl_or_b32 v171, v2, 10, v3
	s_or_b32 s26, s29, s3
	v_bitop3_b32 v179, v171, s26, v170 bitop3:0x36
	s_or_b32 s5, s26, 0x280
	v_bitop3_b32 v178, v171, s5, v170 bitop3:0x36
	s_or_b32 s30, s3, 0x800
	s_or_b32 s33, s3, 0x1000
	s_or_b32 s29, s29, 64
	s_or_b32 s34, s29, s33
	v_bitop3_b32 v180, v171, s34, v170 bitop3:0x36
	s_or_b32 s29, s3, s29
	s_or_b32 s29, s29, 0x1280
	s_and_b32 s5, s2, 1
	s_lshl_b32 s31, s5, 4
	s_or_b32 s2, s31, s3
	v_bitop3_b32 v173, v171, s2, v170 bitop3:0x36
	v_bitop3_b32 v34, v156, 31, v156 bitop3:0xc
	v_lshrrev_b32_e32 v35, 4, v34
	v_bitop3_b32 v36, v34, v182, 1 bitop3:0x6c
	v_xor_b32_e32 v36, v36, v35
	v_bitop3_b32 v34, v34, v154, 4 bitop3:0x6c
	v_bitop3_b32 v37, v156, 10, 31 bitop3:8
	v_or3_b32 v34, v37, v34, v36
	v_lshlrev_b32_e32 v35, 10, v35
	v_lshlrev_b32_e32 v34, 4, v34
	v_or3_b32 v154, v35, v34, v170
	v_bitop3_b32 v172, s2, v154, v159 bitop3:0x36
	v_bitop3_b32 v176, v171, s29, v170 bitop3:0x36
	s_or_b32 s29, s31, s30
	s_or_b32 s29, s29, 0xa0
	v_bitop3_b32 v175, v171, s29, v170 bitop3:0x36
	s_or_b32 s29, s2, 0xaa0
	s_xor_b32 s29, s29, 0x80
	v_xor_b32_e32 v174, s29, v154
	s_or_b32 s29, s26, 0x18e0
	v_bitop3_b32 v181, v171, s29, v170 bitop3:0x36
	s_or_b32 s29, s26, 0x1a60
	v_bitop3_b32 v177, v171, s29, v170 bitop3:0x36
	s_or_b32 s29, s31, 64
	s_or_b32 s3, s3, s29
	s_mov_b32 s41, s3
	s_or_b32 s29, s29, s33
	s_mov_b32 s40, s29
	s_or_b32 s3, s2, 0x18e0
	s_mov_b32 s42, s3
	s_or_b32 s2, s2, 0x1ae0
	s_xor_b32 s2, s2, 0x80
	s_mov_b32 s43, s2
	s_lshr_b32 s38, s4, 1
	v_and_b32_e32 v26, 31, v167
	v_and_b32_e32 v27, 3, v167
	v_bfe_u32 v28, v167, 3, 1
	v_bfe_u32 v29, v167, 2, 1
	v_lshl_or_b32 v27, v28, 2, v27
	v_lshl_or_b32 v27, v29, 3, v27
	v_lshlrev_b32_e32 v32, 9, v182
	v_lshl_add_u32 v30, v27, 3, v32
	v_add_u32_e32 v30, 0x10000, v30
	v_lshl_add_u32 v31, v26, 3, v32
	v_add_u32_e32 v31, 0x10400, v31
	v_xor_b32_e32 v28, 31, v26
	v_lshl_add_u32 v28, v28, 3, v32
	v_add_u32_e32 v28, 0x10400, v28
	v_bfe_u32 v29, v167, 4, 1
	v_mul_u32_u24_e32 v29, 0x78, v29
	v_xor_b32_e32 v254, s38, v29
	v_or_b32_e32 v254, 0x10800, v254
	v_and_b32_e32 v33, 16, v167
	v_cmp_eq_u32_e32 vcc, 0, v33
	ds_read2_b64 v[66:69], v30 offset0:0 offset1:32
	ds_read2_b64 v[70:73], v30 offset0:16 offset1:48
	ds_read2_b64 v[198:201], v31 offset0:0 offset1:32
	ds_read2_b64 v[202:205], v28 offset0:0 offset1:32
	ds_read2_b64 v[206:209], v254 offset0:0 offset1:16
	ds_read2_b64 v[210:213], v254 offset0:32 offset1:48
	s_waitcnt lgkmcnt(0)
	v_cndmask_b32_e32 v74, v67, v66, vcc
	v_cndmask_b32_e32 v75, v69, v68, vcc
	v_cndmask_b32_e64 v76, v66, -v67, vcc
	v_cndmask_b32_e64 v77, v68, -v69, vcc
	v_cndmask_b32_e32 v78, v71, v70, vcc
	v_cndmask_b32_e32 v79, v73, v72, vcc
	v_cndmask_b32_e64 v80, v70, -v71, vcc
	v_cndmask_b32_e64 v81, v72, -v73, vcc
	v_cvt_pk_f16_f32 v190, v74, v75
	v_cvt_pk_f16_f32 v191, v74, v75
	v_cvt_pk_f16_f32 v192, v76, v77
	v_cvt_pk_f16_f32 v193, v76, v77
	v_cvt_pk_f16_f32 v194, v78, v79
	v_cvt_pk_f16_f32 v195, v78, v79
	v_cvt_pk_f16_f32 v196, v80, v81
	v_cvt_pk_f16_f32 v197, v80, v81
	v_mul_f32_e32 v66, v199, v207
	v_mul_f32_e32 v68, v199, v206
	v_mul_f32_e32 v67, v199, v209
	v_mul_f32_e32 v69, v199, v208
	v_fma_f32 v66, v198, v206, -v66
	v_fma_f32 v68, v198, v207, v68
	v_fma_f32 v67, v198, v208, -v67
	v_fma_f32 v69, v198, v209, v69
	v_cvt_pk_f16_f32 v214, v66, v67
	v_cvt_pk_f16_f32 v216, v68, v69
	v_mul_f32_e32 v70, v201, v211
	v_mul_f32_e32 v72, v201, v210
	v_mul_f32_e32 v71, v201, v213
	v_mul_f32_e32 v73, v201, v212
	v_fma_f32 v70, v200, v210, -v70
	v_fma_f32 v72, v200, v211, v72
	v_fma_f32 v71, v200, v212, -v71
	v_fma_f32 v73, v200, v213, v73
	v_cvt_pk_f16_f32 v215, v70, v71
	v_cvt_pk_f16_f32 v217, v72, v73
	v_mul_f32_e32 v66, v203, v207
	v_mul_f32_e32 v68, v203, v206
	v_mul_f32_e32 v67, v203, v209
	v_mul_f32_e32 v69, v203, v208
	v_fma_f32 v66, v202, v206, -v66
	v_fma_f32 v68, v202, v207, v68
	v_fma_f32 v67, v202, v208, -v67
	v_fma_f32 v69, v202, v209, v69
	v_cvt_pk_f16_f32 v218, v66, v67
	v_cvt_pk_f16_f32 v220, v68, v69
	v_mul_f32_e32 v70, v205, v211
	v_mul_f32_e32 v72, v205, v210
	v_mul_f32_e32 v71, v205, v213
	v_mul_f32_e32 v73, v205, v212
	v_fma_f32 v70, v204, v210, -v70
	v_fma_f32 v72, v204, v211, v72
	v_fma_f32 v71, v204, v212, -v71
	v_fma_f32 v73, v204, v213, v73
	v_cvt_pk_f16_f32 v219, v70, v71
	v_cvt_pk_f16_f32 v221, v72, v73
	v_xor_b32_e32 v255, 8, v254
	ds_read2_b64 v[206:209], v255 offset0:0 offset1:16
	ds_read2_b64 v[210:213], v255 offset0:32 offset1:48
	v_mfma_f32_32x32x16_f16 v[2:17], v[190:193], v[214:217], 0
	v_mfma_f32_32x32x16_f16 v[18:33], v[194:197], v[218:221], 0
	s_waitcnt lgkmcnt(0)
	v_mul_f32_e32 v66, v199, v207
	v_mul_f32_e32 v68, v199, v206
	v_mul_f32_e32 v67, v199, v209
	v_mul_f32_e32 v69, v199, v208
	v_fma_f32 v66, v198, v206, -v66
	v_fma_f32 v68, v198, v207, v68
	v_fma_f32 v67, v198, v208, -v67
	v_fma_f32 v69, v198, v209, v69
	v_cvt_pk_f16_f32 v214, v66, v67
	v_cvt_pk_f16_f32 v216, v68, v69
	v_mul_f32_e32 v70, v201, v211
	v_mul_f32_e32 v72, v201, v210
	v_mul_f32_e32 v71, v201, v213
	v_mul_f32_e32 v73, v201, v212
	v_fma_f32 v70, v200, v210, -v70
	v_fma_f32 v72, v200, v211, v72
	v_fma_f32 v71, v200, v212, -v71
	v_fma_f32 v73, v200, v213, v73
	v_cvt_pk_f16_f32 v215, v70, v71
	v_cvt_pk_f16_f32 v217, v72, v73
	v_cvt_pk_f16_f32 v2, v2, v3
	v_cvt_pk_f16_f32 v3, v4, v5
	v_cvt_pk_f16_f32 v4, v6, v7
	v_cvt_pk_f16_f32 v5, v8, v9
	v_cvt_pk_f16_f32 v6, v10, v11
	v_cvt_pk_f16_f32 v7, v12, v13
	v_cvt_pk_f16_f32 v8, v14, v15
	v_cvt_pk_f16_f32 v9, v16, v17
	v_cvt_pk_f16_f32 v18, v18, v19
	v_cvt_pk_f16_f32 v19, v20, v21
	v_cvt_pk_f16_f32 v20, v22, v23
	v_cvt_pk_f16_f32 v21, v24, v25
	v_cvt_pk_f16_f32 v22, v26, v27
	v_cvt_pk_f16_f32 v23, v28, v29
	v_cvt_pk_f16_f32 v24, v30, v31
	v_cvt_pk_f16_f32 v25, v32, v33
	s_setprio 1
	s_waitcnt vmcnt(6)
	v_mul_f32_e32 v66, v203, v207
	v_mul_f32_e32 v68, v203, v206
	v_mfma_f32_32x32x16_f16 v[34:49], v[2:5], v[150:153], 0
	v_mul_f32_e32 v67, v203, v209
	v_mul_f32_e32 v69, v203, v208
	v_mfma_f32_32x32x16_f16 v[34:49], v[18:21], v[146:149], v[34:49]
	v_fma_f32 v66, v202, v206, -v66
	v_fma_f32 v68, v202, v207, v68
	v_mfma_f32_32x32x16_f16 v[34:49], v[6:9], v[142:145], v[34:49]
	v_fma_f32 v67, v202, v208, -v67
	v_fma_f32 v69, v202, v209, v69
	v_mfma_f32_32x32x16_f16 v[34:49], v[22:25], v[138:141], v[34:49]
	v_cvt_pk_f16_f32 v218, v66, v67
	v_cvt_pk_f16_f32 v220, v68, v69
	s_waitcnt vmcnt(2)
	v_mul_f32_e32 v70, v205, v211
	v_mul_f32_e32 v72, v205, v210
	v_mfma_f32_32x32x16_f16 v[50:65], v[2:5], v[134:137], 0
	v_mul_f32_e32 v71, v205, v213
	v_mul_f32_e32 v73, v205, v212
	v_mfma_f32_32x32x16_f16 v[50:65], v[18:21], v[126:129], v[50:65]
	v_fma_f32 v70, v204, v210, -v70
	v_fma_f32 v72, v204, v211, v72
	v_mfma_f32_32x32x16_f16 v[50:65], v[6:9], v[122:125], v[50:65]
	v_fma_f32 v71, v204, v212, -v71
	v_fma_f32 v73, v204, v213, v73
	v_mfma_f32_32x32x16_f16 v[50:65], v[22:25], v[130:133], v[50:65]
	v_cvt_pk_f16_f32 v219, v70, v71
	v_cvt_pk_f16_f32 v221, v72, v73
	v_xor_b32_e32 v255, 16, v254
	ds_read2_b64 v[206:209], v255 offset0:0 offset1:16
	ds_read2_b64 v[210:213], v255 offset0:32 offset1:48
	v_mfma_f32_32x32x16_f16 v[2:17], v[190:193], v[214:217], 0
	v_mfma_f32_32x32x16_f16 v[18:33], v[194:197], v[218:221], 0
	v_cvt_pk_f16_f32 v34, v34, v35
	v_cvt_pk_f16_f32 v35, v36, v37
	v_cvt_pk_f16_f32 v36, v38, v39
	v_cvt_pk_f16_f32 v37, v40, v41
	v_cvt_pk_f16_f32 v38, v42, v43
	v_cvt_pk_f16_f32 v39, v44, v45
	v_cvt_pk_f16_f32 v40, v46, v47
	v_cvt_pk_f16_f32 v41, v48, v49
	v_cvt_pk_f16_f32 v50, v50, v51
	v_cvt_pk_f16_f32 v51, v52, v53
	v_cvt_pk_f16_f32 v52, v54, v55
	v_cvt_pk_f16_f32 v53, v56, v57
	v_cvt_pk_f16_f32 v54, v58, v59
	v_cvt_pk_f16_f32 v55, v60, v61
	v_cvt_pk_f16_f32 v56, v62, v63
	v_cvt_pk_f16_f32 v57, v64, v65
	s_waitcnt vmcnt(2)
	v_cvt_pk_f16_f32 v2, v2, v3
	v_cvt_pk_f16_f32 v3, v4, v5
	v_cvt_pk_f16_f32 v4, v6, v7
	v_cvt_pk_f16_f32 v5, v8, v9
	v_mfma_f32_32x32x16_f16 v[90:105], v[34:37], v[222:225], 0
	v_cvt_pk_f16_f32 v6, v10, v11
	v_cvt_pk_f16_f32 v7, v12, v13
	v_cvt_pk_f16_f32 v8, v14, v15
	v_cvt_pk_f16_f32 v9, v16, v17
	v_mfma_f32_32x32x16_f16 v[106:121], v[34:37], v[238:241], 0
	v_cvt_pk_f16_f32 v18, v18, v19
	v_cvt_pk_f16_f32 v19, v20, v21
	v_cvt_pk_f16_f32 v20, v22, v23
	v_cvt_pk_f16_f32 v21, v24, v25
	v_mfma_f32_32x32x16_f16 v[90:105], v[38:41], v[226:229], v[90:105]
	v_cvt_pk_f16_f32 v22, v26, v27
	v_cvt_pk_f16_f32 v23, v28, v29
	v_cvt_pk_f16_f32 v24, v30, v31
	v_cvt_pk_f16_f32 v25, v32, v33
	v_mfma_f32_32x32x16_f16 v[106:121], v[38:41], v[242:245], v[106:121]
	s_waitcnt lgkmcnt(0)
	v_mul_f32_e32 v66, v199, v207
	v_mul_f32_e32 v68, v199, v206
	v_mul_f32_e32 v67, v199, v209
	v_mfma_f32_32x32x16_f16 v[90:105], v[50:53], v[230:233], v[90:105]
	v_mul_f32_e32 v69, v199, v208
	v_fma_f32 v66, v198, v206, -v66
	v_fma_f32 v68, v198, v207, v68
	v_fma_f32 v67, v198, v208, -v67
	v_mfma_f32_32x32x16_f16 v[106:121], v[50:53], v[246:249], v[106:121]
	v_fma_f32 v69, v198, v209, v69
	v_cvt_pk_f16_f32 v214, v66, v67
	v_cvt_pk_f16_f32 v216, v68, v69
	v_mul_f32_e32 v70, v201, v211
	v_mfma_f32_32x32x16_f16 v[90:105], v[54:57], v[234:237], v[90:105]
	v_mul_f32_e32 v72, v201, v210
	v_mul_f32_e32 v71, v201, v213
	v_mul_f32_e32 v73, v201, v212
	v_fma_f32 v70, v200, v210, -v70
	v_mfma_f32_32x32x16_f16 v[106:121], v[54:57], v[250:253], v[106:121]
	v_fma_f32 v72, v200, v211, v72
	v_fma_f32 v71, v200, v212, -v71
	v_fma_f32 v73, v200, v213, v73
	v_cvt_pk_f16_f32 v215, v70, v71
	v_cvt_pk_f16_f32 v217, v72, v73
	v_mfma_f32_32x32x16_f16 v[34:49], v[2:5], v[150:153], 0
	v_mul_f32_e32 v66, v203, v207
	v_mul_f32_e32 v68, v203, v206
	v_mul_f32_e32 v67, v203, v209
	v_mul_f32_e32 v69, v203, v208
	v_fma_f32 v66, v202, v206, -v66
	v_mfma_f32_32x32x16_f16 v[34:49], v[18:21], v[146:149], v[34:49]
	v_fma_f32 v68, v202, v207, v68
	v_fma_f32 v67, v202, v208, -v67
	v_fma_f32 v69, v202, v209, v69
	v_cvt_pk_f16_f32 v218, v66, v67
	v_cvt_pk_f16_f32 v220, v68, v69
	v_mfma_f32_32x32x16_f16 v[34:49], v[6:9], v[142:145], v[34:49]
	v_mul_f32_e32 v70, v205, v211
	v_mul_f32_e32 v72, v205, v210
	v_mul_f32_e32 v71, v205, v213
	v_mul_f32_e32 v73, v205, v212
	v_fma_f32 v70, v204, v210, -v70
	v_mfma_f32_32x32x16_f16 v[34:49], v[22:25], v[138:141], v[34:49]
	v_fma_f32 v72, v204, v211, v72
	v_fma_f32 v71, v204, v212, -v71
	v_fma_f32 v73, v204, v213, v73
	v_cvt_pk_f16_f32 v219, v70, v71
	v_cvt_pk_f16_f32 v221, v72, v73
	v_mfma_f32_32x32x16_f16 v[50:65], v[2:5], v[134:137], 0
	v_cvt_pk_f16_f32 v90, v90, v91
	v_cvt_pk_f16_f32 v91, v92, v93
	v_cvt_pk_f16_f32 v92, v94, v95
	v_cvt_pk_f16_f32 v93, v96, v97
	v_cvt_pk_f16_f32 v94, v98, v99
	v_mfma_f32_32x32x16_f16 v[50:65], v[18:21], v[126:129], v[50:65]
	v_cvt_pk_f16_f32 v95, v100, v101
	v_cvt_pk_f16_f32 v96, v102, v103
	v_cvt_pk_f16_f32 v97, v104, v105
	v_cvt_pk_f16_f32 v106, v106, v107
	v_cvt_pk_f16_f32 v107, v108, v109
	v_mfma_f32_32x32x16_f16 v[50:65], v[6:9], v[122:125], v[50:65]
	v_cvt_pk_f16_f32 v108, v110, v111
	v_cvt_pk_f16_f32 v109, v112, v113
	v_cvt_pk_f16_f32 v110, v114, v115
	v_cvt_pk_f16_f32 v111, v116, v117
	v_cvt_pk_f16_f32 v112, v118, v119
	v_mfma_f32_32x32x16_f16 v[50:65], v[22:25], v[130:133], v[50:65]
	v_cvt_pk_f16_f32 v113, v120, v121
	ds_write_b128 v173, v[90:93]
	ds_write_b128 v172, v[94:97]
	ds_write_b128 v173, v[106:109] offset:32768
	ds_write_b128 v172, v[110:113] offset:32768
	v_xor_b32_e32 v255, 24, v254
	ds_read2_b64 v[206:209], v255 offset0:0 offset1:16
	ds_read2_b64 v[210:213], v255 offset0:32 offset1:48
	v_mfma_f32_32x32x16_f16 v[2:17], v[190:193], v[214:217], 0
	v_mfma_f32_32x32x16_f16 v[18:33], v[194:197], v[218:221], 0
	v_cvt_pk_f16_f32 v34, v34, v35
	v_cvt_pk_f16_f32 v35, v36, v37
	v_cvt_pk_f16_f32 v36, v38, v39
	v_cvt_pk_f16_f32 v37, v40, v41
	v_cvt_pk_f16_f32 v38, v42, v43
	v_cvt_pk_f16_f32 v39, v44, v45
	v_cvt_pk_f16_f32 v40, v46, v47
	v_cvt_pk_f16_f32 v41, v48, v49
	v_cvt_pk_f16_f32 v50, v50, v51
	v_cvt_pk_f16_f32 v51, v52, v53
	v_cvt_pk_f16_f32 v52, v54, v55
	v_cvt_pk_f16_f32 v53, v56, v57
	v_cvt_pk_f16_f32 v54, v58, v59
	v_cvt_pk_f16_f32 v55, v60, v61
	v_cvt_pk_f16_f32 v56, v62, v63
	v_cvt_pk_f16_f32 v57, v64, v65
	v_mfma_f32_32x32x16_f16 v[90:105], v[34:37], v[222:225], 0
	v_cvt_pk_f16_f32 v2, v2, v3
	v_cvt_pk_f16_f32 v3, v4, v5
	v_cvt_pk_f16_f32 v4, v6, v7
	v_cvt_pk_f16_f32 v5, v8, v9
	v_mfma_f32_32x32x16_f16 v[106:121], v[34:37], v[238:241], 0
	v_cvt_pk_f16_f32 v6, v10, v11
	v_cvt_pk_f16_f32 v7, v12, v13
	v_cvt_pk_f16_f32 v8, v14, v15
	v_cvt_pk_f16_f32 v9, v16, v17
	v_cvt_pk_f16_f32 v18, v18, v19
	v_mfma_f32_32x32x16_f16 v[90:105], v[38:41], v[226:229], v[90:105]
	v_cvt_pk_f16_f32 v19, v20, v21
	v_cvt_pk_f16_f32 v20, v22, v23
	v_cvt_pk_f16_f32 v21, v24, v25
	v_cvt_pk_f16_f32 v22, v26, v27
	v_mfma_f32_32x32x16_f16 v[106:121], v[38:41], v[242:245], v[106:121]
	v_cvt_pk_f16_f32 v23, v28, v29
	v_cvt_pk_f16_f32 v24, v30, v31
	v_cvt_pk_f16_f32 v25, v32, v33
	s_waitcnt lgkmcnt(0)
	v_mul_f32_e32 v66, v199, v207
	v_mfma_f32_32x32x16_f16 v[90:105], v[50:53], v[230:233], v[90:105]
	v_mul_f32_e32 v68, v199, v206
	v_mul_f32_e32 v67, v199, v209
	v_mul_f32_e32 v69, v199, v208
	v_fma_f32 v66, v198, v206, -v66
	v_fma_f32 v68, v198, v207, v68
	v_mfma_f32_32x32x16_f16 v[106:121], v[50:53], v[246:249], v[106:121]
	v_fma_f32 v67, v198, v208, -v67
	v_fma_f32 v69, v198, v209, v69
	v_cvt_pk_f16_f32 v214, v66, v67
	v_cvt_pk_f16_f32 v216, v68, v69
	v_mfma_f32_32x32x16_f16 v[90:105], v[54:57], v[234:237], v[90:105]
	v_mul_f32_e32 v70, v201, v211
	v_mul_f32_e32 v72, v201, v210
	v_mul_f32_e32 v71, v201, v213
	v_mul_f32_e32 v73, v201, v212
	v_fma_f32 v70, v200, v210, -v70
	v_mfma_f32_32x32x16_f16 v[106:121], v[54:57], v[250:253], v[106:121]
	v_fma_f32 v72, v200, v211, v72
	v_fma_f32 v71, v200, v212, -v71
	v_fma_f32 v73, v200, v213, v73
	v_cvt_pk_f16_f32 v215, v70, v71
	v_cvt_pk_f16_f32 v217, v72, v73
	v_mfma_f32_32x32x16_f16 v[34:49], v[2:5], v[150:153], 0
	v_mul_f32_e32 v66, v203, v207
	v_mul_f32_e32 v68, v203, v206
	v_mul_f32_e32 v67, v203, v209
	v_mul_f32_e32 v69, v203, v208
	v_fma_f32 v66, v202, v206, -v66
	v_mfma_f32_32x32x16_f16 v[34:49], v[18:21], v[146:149], v[34:49]
	v_fma_f32 v68, v202, v207, v68
	v_fma_f32 v67, v202, v208, -v67
	v_fma_f32 v69, v202, v209, v69
	v_cvt_pk_f16_f32 v218, v66, v67
	v_cvt_pk_f16_f32 v220, v68, v69
	v_mfma_f32_32x32x16_f16 v[34:49], v[6:9], v[142:145], v[34:49]
	v_mul_f32_e32 v70, v205, v211
	v_mul_f32_e32 v72, v205, v210
	v_mul_f32_e32 v71, v205, v213
	v_mul_f32_e32 v73, v205, v212
	v_fma_f32 v70, v204, v210, -v70
	v_mfma_f32_32x32x16_f16 v[34:49], v[22:25], v[138:141], v[34:49]
	v_fma_f32 v72, v204, v211, v72
	v_fma_f32 v71, v204, v212, -v71
	v_fma_f32 v73, v204, v213, v73
	v_cvt_pk_f16_f32 v219, v70, v71
	v_cvt_pk_f16_f32 v221, v72, v73
	v_cvt_pk_f16_f32 v90, v90, v91
	v_mfma_f32_32x32x16_f16 v[50:65], v[2:5], v[134:137], 0
	v_cvt_pk_f16_f32 v91, v92, v93
	v_cvt_pk_f16_f32 v92, v94, v95
	v_cvt_pk_f16_f32 v93, v96, v97
	v_cvt_pk_f16_f32 v94, v98, v99
	v_cvt_pk_f16_f32 v95, v100, v101
	v_mfma_f32_32x32x16_f16 v[50:65], v[18:21], v[126:129], v[50:65]
	v_cvt_pk_f16_f32 v96, v102, v103
	v_cvt_pk_f16_f32 v97, v104, v105
	v_cvt_pk_f16_f32 v106, v106, v107
	v_cvt_pk_f16_f32 v107, v108, v109
	v_cvt_pk_f16_f32 v108, v110, v111
	v_mfma_f32_32x32x16_f16 v[50:65], v[6:9], v[122:125], v[50:65]
	v_cvt_pk_f16_f32 v109, v112, v113
	v_cvt_pk_f16_f32 v110, v114, v115
	v_cvt_pk_f16_f32 v111, v116, v117
	v_cvt_pk_f16_f32 v112, v118, v119
	v_cvt_pk_f16_f32 v113, v120, v121
	v_mfma_f32_32x32x16_f16 v[50:65], v[22:25], v[130:133], v[50:65]
	v_xor_b32_e32 v74, 0x8a0, v173
	v_xor_b32_e32 v75, 0x8a0, v172
	ds_write_b128 v74, v[90:93]
	ds_write_b128 v75, v[94:97]
	ds_write_b128 v74, v[106:109] offset:32768
	ds_write_b128 v75, v[110:113] offset:32768
	s_nop 0
	v_mfma_f32_32x32x16_f16 v[2:17], v[190:193], v[214:217], 0
	v_mfma_f32_32x32x16_f16 v[18:33], v[194:197], v[218:221], 0
	v_cvt_pk_f16_f32 v34, v34, v35
	v_cvt_pk_f16_f32 v35, v36, v37
	v_cvt_pk_f16_f32 v36, v38, v39
	v_cvt_pk_f16_f32 v37, v40, v41
	v_cvt_pk_f16_f32 v38, v42, v43
	v_cvt_pk_f16_f32 v39, v44, v45
	v_cvt_pk_f16_f32 v40, v46, v47
	v_cvt_pk_f16_f32 v41, v48, v49
	v_cvt_pk_f16_f32 v50, v50, v51
	v_cvt_pk_f16_f32 v51, v52, v53
	v_cvt_pk_f16_f32 v52, v54, v55
	v_cvt_pk_f16_f32 v53, v56, v57
	v_cvt_pk_f16_f32 v54, v58, v59
	v_cvt_pk_f16_f32 v55, v60, v61
	v_cvt_pk_f16_f32 v56, v62, v63
	v_cvt_pk_f16_f32 v57, v64, v65
	v_mfma_f32_32x32x16_f16 v[90:105], v[34:37], v[222:225], 0
	v_cvt_pk_f16_f32 v2, v2, v3
	v_cvt_pk_f16_f32 v3, v4, v5
	v_mfma_f32_32x32x16_f16 v[106:121], v[34:37], v[238:241], 0
	v_cvt_pk_f16_f32 v4, v6, v7
	v_cvt_pk_f16_f32 v5, v8, v9
	v_mfma_f32_32x32x16_f16 v[90:105], v[38:41], v[226:229], v[90:105]
	v_cvt_pk_f16_f32 v6, v10, v11
	v_cvt_pk_f16_f32 v7, v12, v13
	v_mfma_f32_32x32x16_f16 v[106:121], v[38:41], v[242:245], v[106:121]
	v_cvt_pk_f16_f32 v8, v14, v15
	v_cvt_pk_f16_f32 v9, v16, v17
	v_mfma_f32_32x32x16_f16 v[90:105], v[50:53], v[230:233], v[90:105]
	v_cvt_pk_f16_f32 v18, v18, v19
	v_cvt_pk_f16_f32 v19, v20, v21
	v_mfma_f32_32x32x16_f16 v[106:121], v[50:53], v[246:249], v[106:121]
	v_cvt_pk_f16_f32 v20, v22, v23
	v_cvt_pk_f16_f32 v21, v24, v25
	v_mfma_f32_32x32x16_f16 v[90:105], v[54:57], v[234:237], v[90:105]
	v_cvt_pk_f16_f32 v22, v26, v27
	v_cvt_pk_f16_f32 v23, v28, v29
	v_mfma_f32_32x32x16_f16 v[106:121], v[54:57], v[250:253], v[106:121]
	v_cvt_pk_f16_f32 v24, v30, v31
	v_cvt_pk_f16_f32 v25, v32, v33
	v_mfma_f32_32x32x16_f16 v[34:49], v[2:5], v[150:153], 0
	v_mfma_f32_32x32x16_f16 v[34:49], v[18:21], v[146:149], v[34:49]
	v_mfma_f32_32x32x16_f16 v[34:49], v[6:9], v[142:145], v[34:49]
	v_mfma_f32_32x32x16_f16 v[34:49], v[22:25], v[138:141], v[34:49]
	v_mfma_f32_32x32x16_f16 v[50:65], v[2:5], v[134:137], 0
	s_nop 5
	v_cvt_pk_f16_f32 v90, v90, v91
	v_cvt_pk_f16_f32 v91, v92, v93
	v_cvt_pk_f16_f32 v92, v94, v95
	v_cvt_pk_f16_f32 v93, v96, v97
	v_mfma_f32_32x32x16_f16 v[50:65], v[18:21], v[126:129], v[50:65]
	v_cvt_pk_f16_f32 v94, v98, v99
	v_cvt_pk_f16_f32 v95, v100, v101
	v_cvt_pk_f16_f32 v96, v102, v103
	v_cvt_pk_f16_f32 v97, v104, v105
	v_cvt_pk_f16_f32 v106, v106, v107
	v_cvt_pk_f16_f32 v107, v108, v109
	v_mfma_f32_32x32x16_f16 v[50:65], v[6:9], v[122:125], v[50:65]
	v_cvt_pk_f16_f32 v108, v110, v111
	v_cvt_pk_f16_f32 v109, v112, v113
	v_cvt_pk_f16_f32 v110, v114, v115
	v_cvt_pk_f16_f32 v111, v116, v117
	v_cvt_pk_f16_f32 v112, v118, v119
	v_cvt_pk_f16_f32 v113, v120, v121
	v_mfma_f32_32x32x16_f16 v[50:65], v[22:25], v[130:133], v[50:65]
	v_xor_b32_e32 v74, 0x1040, v173
	v_xor_b32_e32 v75, 0x1040, v172
	ds_write_b128 v74, v[90:93]
	ds_write_b128 v75, v[94:97]
	ds_write_b128 v74, v[106:109] offset:32768
	ds_write_b128 v75, v[110:113] offset:32768
	s_nop 11
	v_cvt_pk_f16_f32 v34, v34, v35
	v_cvt_pk_f16_f32 v35, v36, v37
	v_cvt_pk_f16_f32 v36, v38, v39
	v_cvt_pk_f16_f32 v37, v40, v41
	v_cvt_pk_f16_f32 v38, v42, v43
	v_cvt_pk_f16_f32 v39, v44, v45
	v_cvt_pk_f16_f32 v40, v46, v47
	v_cvt_pk_f16_f32 v41, v48, v49
	v_cvt_pk_f16_f32 v50, v50, v51
	v_cvt_pk_f16_f32 v51, v52, v53
	v_cvt_pk_f16_f32 v52, v54, v55
	v_cvt_pk_f16_f32 v53, v56, v57
	v_cvt_pk_f16_f32 v54, v58, v59
	v_cvt_pk_f16_f32 v55, v60, v61
	v_cvt_pk_f16_f32 v56, v62, v63
	v_cvt_pk_f16_f32 v57, v64, v65
	v_mfma_f32_32x32x16_f16 v[90:105], v[34:37], v[222:225], 0
	v_mfma_f32_32x32x16_f16 v[106:121], v[34:37], v[238:241], 0
	v_mfma_f32_32x32x16_f16 v[90:105], v[38:41], v[226:229], v[90:105]
	v_mfma_f32_32x32x16_f16 v[106:121], v[38:41], v[242:245], v[106:121]
	v_mfma_f32_32x32x16_f16 v[90:105], v[50:53], v[230:233], v[90:105]
	v_mfma_f32_32x32x16_f16 v[106:121], v[50:53], v[246:249], v[106:121]
	v_mfma_f32_32x32x16_f16 v[90:105], v[54:57], v[234:237], v[90:105]
	v_mfma_f32_32x32x16_f16 v[106:121], v[54:57], v[250:253], v[106:121]
	v_and_b32_e32 v134, 1, v156
	v_bitop3_b32 v132, v171, s40, v170 bitop3:0x36
	v_bitop3_b32 v131, s41, v154, v160 bitop3:0x36
	v_bitop3_b32 v135, v171, s42, v170 bitop3:0x36
	v_xor_b32_e32 v133, s43, v154
	v_and_b32_e32 v130, 4, v156
	s_lshl_b32 s2, s27, 3
	s_lshl_b32 s3, s5, 2
	s_or_b32 s2, s3, s2
	s_ashr_i32 s3, s2, 31
	s_lshl_b64 s[2:3], s[2:3], 13
	s_add_u32 s2, s20, s2
	s_addc_u32 s3, s21, s3
	v_lshlrev_b32_e32 v154, 1, v169
	v_lshl_add_u64 v[2:3], s[2:3], 0, v[154:155]
	v_add_co_u32_e32 v2, vcc, s23, v2
	s_nop 1
	v_addc_co_u32_e32 v3, vcc, 0, v3, vcc
	v_cvt_pk_f16_f32 v90, v90, v91
	v_cvt_pk_f16_f32 v91, v92, v93
	v_cvt_pk_f16_f32 v92, v94, v95
	v_cvt_pk_f16_f32 v93, v96, v97
	v_cvt_pk_f16_f32 v94, v98, v99
	v_cvt_pk_f16_f32 v95, v100, v101
	v_cvt_pk_f16_f32 v96, v102, v103
	v_cvt_pk_f16_f32 v97, v104, v105
	v_cvt_pk_f16_f32 v106, v106, v107
	v_cvt_pk_f16_f32 v107, v108, v109
	v_cvt_pk_f16_f32 v108, v110, v111
	v_cvt_pk_f16_f32 v109, v112, v113
	v_cvt_pk_f16_f32 v110, v114, v115
	v_cvt_pk_f16_f32 v111, v116, v117
	v_cvt_pk_f16_f32 v112, v118, v119
	v_cvt_pk_f16_f32 v113, v120, v121
	v_xor_b32_e32 v74, 0x18e0, v173
	v_xor_b32_e32 v75, 0x18e0, v172
	ds_write_b128 v74, v[90:93]
	ds_write_b128 v75, v[94:97]
	ds_write_b128 v74, v[106:109] offset:32768
	ds_write_b128 v75, v[110:113] offset:32768
	s_setprio 1
	s_waitcnt lgkmcnt(0)
	s_barrier
	global_load_dwordx4 v[62:65], v154, s[2:3]
	global_load_dwordx4 v[46:49], v154, s[2:3] offset:1024
	global_load_dwordx4 v[42:45], v154, s[2:3] offset:2048
	global_load_dwordx4 v[38:41], v154, s[2:3] offset:3072
	global_load_dwordx4 v[54:57], v[2:3], off offset:1024
	global_load_dwordx4 v[50:53], v[2:3], off offset:2048
	v_lshl_add_u64 v[4:5], s[12:13], 0, v[154:155]
	global_load_dwordx4 v[126:129], v154, s[12:13]
	global_load_dwordx4 v[122:125], v154, s[12:13] offset:1024
	global_load_dwordx4 v[118:121], v154, s[12:13] offset:2048
	global_load_dwordx4 v[114:117], v154, s[12:13] offset:3072
	global_load_dwordx4 v[34:37], v168, s[2:3]
	global_load_dwordx4 v[110:113], v168, s[12:13]
	v_add_co_u32_e32 v4, vcc, s23, v4
	s_nop 1
	v_addc_co_u32_e32 v5, vcc, 0, v5, vcc
	global_load_dwordx4 v[58:61], v[2:3], off offset:3072
	global_load_dwordx4 v[106:109], v[4:5], off offset:1024
	global_load_dwordx4 v[94:97], v[4:5], off offset:2048
	global_load_dwordx4 v[90:93], v[4:5], off offset:3072
	v_bfrev_b32_e32 v3, v156
	v_lshlrev_b32_e32 v7, 5, v167
	v_lshlrev_b32_e32 v6, 9, v167
	v_and_b32_e32 v7, 0x200, v7
	v_lshlrev_b32_e32 v8, 8, v167
	v_lshrrev_b32_e32 v3, 27, v3
	v_lshrrev_b32_e32 v2, 2, v167
	v_lshrrev_b32_e32 v4, 4, v156
	v_xor_b32_e32 v5, v169, v156
	v_and_b32_e32 v6, 0x5800, v6
	v_and_b32_e32 v3, 8, v3
	v_and_or_b32 v7, v8, s24, v7
	v_lshrrev_b32_e32 v5, 1, v5
	v_xor_b32_e32 v4, v2, v4
	v_or3_b32 v3, v7, v6, v3
	v_bitop3_b32 v7, v2, v182, 1 bitop3:0x6c
	v_lshlrev_b32_e32 v2, 1, v167
	v_and_b32_e32 v5, 4, v5
	v_lshlrev_b32_e32 v4, 3, v4
	v_lshrrev_b32_e32 v6, 1, v167
	v_and_b32_e32 v2, 2, v2
	v_and_or_b32 v9, v169, 8, v2
	v_and_b32_e32 v2, 8, v4
	v_and_or_b32 v4, v6, 2, v5
	v_or3_b32 v2, v4, v2, v134
	v_lshlrev_b32_e32 v2, 4, v2
	v_bitop3_b32 v146, v3, s28, v2 bitop3:0x36
	v_xor_b32_e32 v8, v6, v182
	v_xor_b32_e32 v147, 0x2010, v146
	v_lshlrev_b32_e32 v8, 2, v8
	v_and_b32_e32 v8, 4, v8
	v_or3_b32 v6, v9, v7, v8
	v_lshlrev_b32_e32 v7, 11, v167
	v_and_b32_e32 v8, 0x7800, v7
	v_lshlrev_b32_e32 v6, 4, v6
	v_or3_b32 v22, v6, v8, v170
	v_and_b32_e32 v23, 0x8000, v7
	v_xor_b32_e32 v150, 16, v146
	v_xad_u32 v70, v22, s28, v23
	v_xor_b32_e32 v151, 0x2000, v146
	ds_read_b64_tr_b16 v[18:19], v146
	ds_read_b64_tr_b16 v[20:21], v147
	ds_read_b64_tr_b16 v[22:23], v146 offset:32768
	ds_read_b64_tr_b16 v[24:25], v147 offset:32768
	ds_read_b64_tr_b16 v[26:27], v150
	ds_read_b64_tr_b16 v[28:29], v151
	ds_read_b64_tr_b16 v[30:31], v150 offset:32768
	ds_read_b64_tr_b16 v[32:33], v151 offset:32768
	v_xor_b32_e32 v148, 32, v146
	v_xor_b32_e32 v149, 0x2030, v146
	v_xor_b32_e32 v144, 48, v146
	v_xor_b32_e32 v145, 0x2020, v146
	v_xor_b32_e32 v142, 64, v146
	v_xor_b32_e32 v143, 0x2050, v146
	v_xor_b32_e32 v140, 0x50, v146
	v_xor_b32_e32 v141, 0x2040, v146
	v_xor_b32_e32 v138, 0x60, v146
	v_xor_b32_e32 v139, 0x2070, v146
	v_xor_b32_e32 v136, 0x70, v146
	v_xor_b32_e32 v137, 0x2060, v146
	v_xor_b32_e32 v71, 0x60, v70
	s_lshl_b64 s[0:1], s[0:1], 13
	s_add_u32 s0, s8, s0
	s_addc_u32 s1, s9, s1
	s_waitcnt vmcnt(17) lgkmcnt(4)
	v_mfma_f32_32x32x16_f16 v[2:17], v[18:21], v[86:89], 0
	s_waitcnt vmcnt(16)
	v_mfma_f32_32x32x16_f16 v[2:17], v[22:25], v[82:85], v[2:17]
	ds_read_b64_tr_b16 v[206:207], v148
	ds_read_b64_tr_b16 v[208:209], v149
	ds_read_b64_tr_b16 v[210:211], v148 offset:32768
	ds_read_b64_tr_b16 v[212:213], v149 offset:32768
	s_waitcnt lgkmcnt(4)
	v_mfma_f32_32x32x16_f16 v[190:205], v[26:29], v[86:89], 0
	v_mfma_f32_32x32x16_f16 v[190:205], v[30:33], v[82:85], v[190:205]
	s_nop 4
	v_cvt_pk_f16_f32 v2, v2, v3
	v_cvt_pk_f16_f32 v3, v4, v5
	v_cvt_pk_f16_f32 v4, v6, v7
	v_cvt_pk_f16_f32 v5, v8, v9
	v_cvt_pk_f16_f32 v6, v10, v11
	v_cvt_pk_f16_f32 v7, v12, v13
	v_cvt_pk_f16_f32 v8, v14, v15
	v_cvt_pk_f16_f32 v9, v16, v17
	v_xor_b32_e32 v73, 0x280, v70
	ds_write_b128 v70, v[2:5]
	ds_write_b128 v73, v[6:9]
	ds_read_b64_tr_b16 v[18:19], v144
	ds_read_b64_tr_b16 v[20:21], v145
	ds_read_b64_tr_b16 v[22:23], v144 offset:32768
	ds_read_b64_tr_b16 v[24:25], v145 offset:32768
	s_waitcnt lgkmcnt(6)
	v_mfma_f32_32x32x16_f16 v[2:17], v[206:209], v[86:89], 0
	v_mfma_f32_32x32x16_f16 v[2:17], v[210:213], v[82:85], v[2:17]
	v_cvt_pk_f16_f32 v190, v190, v191
	v_cvt_pk_f16_f32 v191, v192, v193
	v_cvt_pk_f16_f32 v192, v194, v195
	v_cvt_pk_f16_f32 v193, v196, v197
	v_cvt_pk_f16_f32 v194, v198, v199
	v_cvt_pk_f16_f32 v195, v200, v201
	v_cvt_pk_f16_f32 v196, v202, v203
	v_cvt_pk_f16_f32 v197, v204, v205
	v_xor_b32_e32 v72, 16, v70
	v_xor_b32_e32 v73, 0x290, v70
	ds_write_b128 v72, v[190:193]
	ds_write_b128 v73, v[194:197]
	ds_read_b64_tr_b16 v[26:27], v142
	ds_read_b64_tr_b16 v[28:29], v143
	ds_read_b64_tr_b16 v[30:31], v142 offset:32768
	ds_read_b64_tr_b16 v[32:33], v143 offset:32768
	s_waitcnt lgkmcnt(6)
	v_mfma_f32_32x32x16_f16 v[190:205], v[18:21], v[86:89], 0
	v_mfma_f32_32x32x16_f16 v[190:205], v[22:25], v[82:85], v[190:205]
	v_cvt_pk_f16_f32 v2, v2, v3
	v_cvt_pk_f16_f32 v3, v4, v5
	v_cvt_pk_f16_f32 v4, v6, v7
	v_cvt_pk_f16_f32 v5, v8, v9
	v_cvt_pk_f16_f32 v6, v10, v11
	v_cvt_pk_f16_f32 v7, v12, v13
	v_cvt_pk_f16_f32 v8, v14, v15
	v_cvt_pk_f16_f32 v9, v16, v17
	v_xor_b32_e32 v72, 32, v70
	v_xor_b32_e32 v73, 0x2a0, v70
	ds_write_b128 v72, v[2:5]
	ds_write_b128 v73, v[6:9]
	ds_read_b64_tr_b16 v[206:207], v140
	ds_read_b64_tr_b16 v[208:209], v141
	ds_read_b64_tr_b16 v[210:211], v140 offset:32768
	ds_read_b64_tr_b16 v[212:213], v141 offset:32768
	s_waitcnt lgkmcnt(6)
	v_mfma_f32_32x32x16_f16 v[2:17], v[26:29], v[86:89], 0
	v_mfma_f32_32x32x16_f16 v[2:17], v[30:33], v[82:85], v[2:17]
	v_cvt_pk_f16_f32 v190, v190, v191
	v_cvt_pk_f16_f32 v191, v192, v193
	v_cvt_pk_f16_f32 v192, v194, v195
	v_cvt_pk_f16_f32 v193, v196, v197
	v_cvt_pk_f16_f32 v194, v198, v199
	v_cvt_pk_f16_f32 v195, v200, v201
	v_cvt_pk_f16_f32 v196, v202, v203
	v_cvt_pk_f16_f32 v197, v204, v205
	v_xor_b32_e32 v72, 48, v70
	v_xor_b32_e32 v73, 0x2b0, v70
	ds_write_b128 v72, v[190:193]
	ds_write_b128 v73, v[194:197]
	ds_read_b64_tr_b16 v[18:19], v138
	ds_read_b64_tr_b16 v[20:21], v139
	ds_read_b64_tr_b16 v[22:23], v138 offset:32768
	ds_read_b64_tr_b16 v[24:25], v139 offset:32768
	s_waitcnt lgkmcnt(6)
	v_mfma_f32_32x32x16_f16 v[190:205], v[206:209], v[86:89], 0
	v_mfma_f32_32x32x16_f16 v[190:205], v[210:213], v[82:85], v[190:205]
	v_cvt_pk_f16_f32 v2, v2, v3
	v_cvt_pk_f16_f32 v3, v4, v5
	v_cvt_pk_f16_f32 v4, v6, v7
	v_cvt_pk_f16_f32 v5, v8, v9
	v_cvt_pk_f16_f32 v6, v10, v11
	v_cvt_pk_f16_f32 v7, v12, v13
	v_cvt_pk_f16_f32 v8, v14, v15
	v_cvt_pk_f16_f32 v9, v16, v17
	v_xor_b32_e32 v72, 64, v70
	v_xor_b32_e32 v73, 0x2c0, v70
	ds_write_b128 v72, v[2:5]
	ds_write_b128 v73, v[6:9]
	ds_read_b64_tr_b16 v[26:27], v136
	ds_read_b64_tr_b16 v[28:29], v137
	ds_read_b64_tr_b16 v[30:31], v136 offset:32768
	ds_read_b64_tr_b16 v[32:33], v137 offset:32768
	s_waitcnt lgkmcnt(6)
	v_mfma_f32_32x32x16_f16 v[2:17], v[18:21], v[86:89], 0
	v_mfma_f32_32x32x16_f16 v[2:17], v[22:25], v[82:85], v[2:17]
	v_cvt_pk_f16_f32 v190, v190, v191
	v_cvt_pk_f16_f32 v191, v192, v193
	v_cvt_pk_f16_f32 v192, v194, v195
	v_cvt_pk_f16_f32 v193, v196, v197
	v_cvt_pk_f16_f32 v194, v198, v199
	v_cvt_pk_f16_f32 v195, v200, v201
	v_cvt_pk_f16_f32 v196, v202, v203
	v_cvt_pk_f16_f32 v197, v204, v205
	v_xor_b32_e32 v72, 0x50, v70
	v_xor_b32_e32 v73, 0x2d0, v70
	ds_write_b128 v72, v[190:193]
	ds_write_b128 v73, v[194:197]
	s_waitcnt lgkmcnt(2)
	v_mfma_f32_32x32x16_f16 v[190:205], v[26:29], v[86:89], 0
	v_mfma_f32_32x32x16_f16 v[190:205], v[30:33], v[82:85], v[190:205]
	v_cvt_pk_f16_f32 v2, v2, v3
	v_cvt_pk_f16_f32 v3, v4, v5
	v_cvt_pk_f16_f32 v4, v6, v7
	v_cvt_pk_f16_f32 v5, v8, v9
	v_cvt_pk_f16_f32 v6, v10, v11
	v_cvt_pk_f16_f32 v7, v12, v13
	v_cvt_pk_f16_f32 v8, v14, v15
	v_cvt_pk_f16_f32 v9, v16, v17
	v_xor_b32_e32 v72, 0x60, v70
	v_xor_b32_e32 v73, 0x2e0, v70
	ds_write_b128 v72, v[2:5]
	ds_write_b128 v73, v[6:9]
	v_cvt_pk_f16_f32 v190, v190, v191
	v_cvt_pk_f16_f32 v191, v192, v193
	v_cvt_pk_f16_f32 v192, v194, v195
	v_cvt_pk_f16_f32 v193, v196, v197
	v_cvt_pk_f16_f32 v194, v198, v199
	v_cvt_pk_f16_f32 v195, v200, v201
	v_cvt_pk_f16_f32 v196, v202, v203
	v_cvt_pk_f16_f32 v197, v204, v205
	v_xor_b32_e32 v72, 0x70, v70
	v_xor_b32_e32 v73, 0x2f0, v70
	ds_write_b128 v72, v[190:193]
	ds_write_b128 v73, v[194:197]
	v_lshl_add_u64 v[2:3], s[0:1], 0, v[154:155]
	v_lshl_add_u64 v[4:5], v[2:3], 0, s[18:19]
	v_add_co_u32_e32 v2, vcc, s25, v2
	s_waitcnt lgkmcnt(0)
	s_nop 0
	v_addc_co_u32_e32 v3, vcc, 0, v3, vcc
	s_barrier
	s_nop 0
	s_nop 0
	global_load_dwordx4 v[102:105], v[2:3], off
	global_load_dwordx4 v[98:101], v[4:5], off offset:1024
	s_setprio 1
	s_add_u32 s0, s2, 0x2000
	s_addc_u32 s1, s3, 0
	v_lshl_add_u64 v[2:3], s[0:1], 0, v[154:155]
	v_add_co_u32_e32 v2, vcc, s23, v2
	global_load_dwordx4 v[66:69], v154, s[0:1]
	global_load_dwordx4 v[70:73], v154, s[0:1] offset:1024
	global_load_dwordx4 v[74:77], v154, s[0:1] offset:2048
	global_load_dwordx4 v[78:81], v154, s[0:1] offset:3072
	v_addc_co_u32_e32 v3, vcc, 0, v3, vcc
	global_load_dwordx4 v[82:85], v168, s[0:1]
	global_load_dwordx4 v[86:89], v[2:3], off offset:1024
	global_load_dwordx4 v[182:185], v[2:3], off offset:2048
	global_load_dwordx4 v[186:189], v[2:3], off offset:3072
	ds_read_b128 v[18:21], v179
	ds_read_b128 v[22:25], v179 offset:32768
	ds_read_b128 v[26:29], v178
	ds_read_b128 v[30:33], v178 offset:32768
	s_add_u32 s0, s2, 0x6000
	s_addc_u32 s1, s3, 0
	s_waitcnt vmcnt(25) lgkmcnt(3)
	v_mfma_f32_32x32x16_f16 v[2:17], v[18:21], v[62:65], 0
	s_add_u32 s2, s2, 0x4000
	s_addc_u32 s3, s3, 0
	s_or_b32 s27, s26, 0x8a0
	s_or_b32 s26, s26, 0xa20
	s_waitcnt vmcnt(24) lgkmcnt(1)
	v_mfma_f32_32x32x16_f16 v[2:17], v[26:29], v[46:49], v[2:17]
	s_waitcnt vmcnt(23)
	v_mfma_f32_32x32x16_f16 v[2:17], v[22:25], v[42:45], v[2:17]
	s_waitcnt vmcnt(22) lgkmcnt(0)
	v_mfma_f32_32x32x16_f16 v[2:17], v[30:33], v[38:41], v[2:17]
	s_waitcnt vmcnt(15)
	v_mfma_f32_32x32x16_f16 v[34:49], v[18:21], v[34:37], 0
	s_nop 9
	v_cvt_pk_f16_f32 v9, v8, v9
	v_cvt_pk_f16_f32 v8, v6, v7
	v_cvt_pk_f16_f32 v7, v4, v5
	v_cvt_pk_f16_f32 v6, v2, v3
	v_cvt_pk_f16_f32 v5, v16, v17
	v_cvt_pk_f16_f32 v4, v14, v15
	v_cvt_pk_f16_f32 v3, v12, v13
	v_mfma_f32_32x32x16_f16 v[34:49], v[26:29], v[54:57], v[34:49]
	v_cvt_pk_f16_f32 v2, v10, v11
	v_mfma_f32_32x32x16_f16 v[34:49], v[22:25], v[50:53], v[34:49]
	s_waitcnt vmcnt(13)
	v_mfma_f32_32x32x16_f16 v[34:49], v[30:33], v[58:61], v[34:49]
	v_mfma_f32_32x32x16_f16 v[18:33], v[6:9], v[126:129], 0
	s_nop 10
	v_cvt_pk_f16_f32 v13, v40, v41
	v_cvt_pk_f16_f32 v12, v38, v39
	v_cvt_pk_f16_f32 v11, v36, v37
	v_cvt_pk_f16_f32 v10, v34, v35
	v_cvt_pk_f16_f32 v17, v48, v49
	v_cvt_pk_f16_f32 v16, v46, v47
	v_cvt_pk_f16_f32 v15, v44, v45
	v_mfma_f32_32x32x16_f16 v[50:65], v[6:9], v[110:113], 0
	v_bitop3_b32 v6, v171, s27, v170 bitop3:0x36
	v_cvt_pk_f16_f32 v14, v42, v43
	v_mfma_f32_32x32x16_f16 v[18:33], v[2:5], v[122:125], v[18:33]
	s_waitcnt vmcnt(12)
	v_mfma_f32_32x32x16_f16 v[50:65], v[2:5], v[106:109], v[50:65]
	ds_read_b128 v[2:5], v6
	ds_read_b128 v[6:9], v6 offset:32768
	v_mfma_f32_32x32x16_f16 v[18:33], v[10:13], v[118:121], v[18:33]
	s_waitcnt vmcnt(11)
	v_mfma_f32_32x32x16_f16 v[50:65], v[10:13], v[94:97], v[50:65]
	s_waitcnt vmcnt(7) lgkmcnt(1)
	v_mfma_f32_32x32x16_f16 v[34:49], v[2:5], v[66:69], 0
	v_mfma_f32_32x32x16_f16 v[18:33], v[14:17], v[114:117], v[18:33]
	v_mfma_f32_32x32x16_f16 v[50:65], v[14:17], v[90:93], v[50:65]
	v_bitop3_b32 v14, v171, s26, v170 bitop3:0x36
	ds_read_b128 v[10:13], v14
	ds_read_b128 v[14:17], v14 offset:32768
	s_nop 7
	v_cvt_pk_f16_f32 v25, v24, v25
	v_cvt_pk_f16_f32 v24, v22, v23
	v_cvt_pk_f16_f32 v23, v20, v21
	v_cvt_pk_f16_f32 v22, v18, v19
	v_cvt_pk_f16_f32 v21, v32, v33
	s_waitcnt vmcnt(6) lgkmcnt(1)
	v_mfma_f32_32x32x16_f16 v[34:49], v[10:13], v[70:73], v[34:49]
	v_cvt_pk_f16_f32 v20, v30, v31
	v_cvt_pk_f16_f32 v19, v28, v29
	v_cvt_pk_f16_f32 v18, v26, v27
	ds_write_b128 v173, v[22:25]
	ds_write_b128 v172, v[18:21]
	v_cvt_pk_f16_f32 v21, v56, v57
	v_cvt_pk_f16_f32 v20, v54, v55
	s_waitcnt vmcnt(5)
	v_mfma_f32_32x32x16_f16 v[34:49], v[6:9], v[74:77], v[34:49]
	v_cvt_pk_f16_f32 v19, v52, v53
	v_cvt_pk_f16_f32 v18, v50, v51
	ds_write_b128 v173, v[18:21] offset:32768
	v_cvt_pk_f16_f32 v21, v64, v65
	v_cvt_pk_f16_f32 v20, v62, v63
	v_cvt_pk_f16_f32 v19, v60, v61
	v_cvt_pk_f16_f32 v18, v58, v59
	s_waitcnt vmcnt(4) lgkmcnt(3)
	v_mfma_f32_32x32x16_f16 v[34:49], v[14:17], v[78:81], v[34:49]
	ds_write_b128 v172, v[18:21] offset:32768
	s_waitcnt vmcnt(3)
	v_mfma_f32_32x32x16_f16 v[66:81], v[2:5], v[82:85], 0
	s_nop 8
	v_cvt_pk_f16_f32 v41, v40, v41
	v_cvt_pk_f16_f32 v40, v38, v39
	v_cvt_pk_f16_f32 v39, v36, v37
	v_cvt_pk_f16_f32 v38, v34, v35
	v_cvt_pk_f16_f32 v85, v48, v49
	v_cvt_pk_f16_f32 v84, v46, v47
	v_cvt_pk_f16_f32 v83, v44, v45
	s_waitcnt vmcnt(2)
	v_mfma_f32_32x32x16_f16 v[66:81], v[10:13], v[86:89], v[66:81]
	v_cvt_pk_f16_f32 v82, v42, v43
	s_waitcnt vmcnt(1)
	v_mfma_f32_32x32x16_f16 v[66:81], v[6:9], v[182:185], v[66:81]
	s_waitcnt vmcnt(0)
	v_mfma_f32_32x32x16_f16 v[66:81], v[14:17], v[186:189], v[66:81]
	v_mfma_f32_32x32x16_f16 v[2:17], v[38:41], v[126:129], 0
	s_nop 10
	v_cvt_pk_f16_f32 v73, v72, v73
	v_cvt_pk_f16_f32 v72, v70, v71
	v_cvt_pk_f16_f32 v70, v66, v67
	v_cvt_pk_f16_f32 v67, v76, v77
	v_cvt_pk_f16_f32 v66, v74, v75
	global_load_dwordx4 v[74:77], v154, s[2:3]
	v_cvt_pk_f16_f32 v71, v68, v69
	v_cvt_pk_f16_f32 v69, v80, v81
	v_cvt_pk_f16_f32 v68, v78, v79
	global_load_dwordx4 v[78:81], v154, s[2:3] offset:1024
	ds_read_b128 v[18:21], v180
	ds_read_b128 v[22:25], v176
	ds_read_b128 v[26:29], v180 offset:32768
	global_load_dwordx4 v[30:33], v154, s[2:3] offset:2048
	v_mfma_f32_32x32x16_f16 v[34:49], v[38:41], v[110:113], 0
	v_mfma_f32_32x32x16_f16 v[2:17], v[82:85], v[122:125], v[2:17]
	v_mfma_f32_32x32x16_f16 v[34:49], v[82:85], v[106:109], v[34:49]
	ds_read_b128 v[82:85], v176 offset:32768
	s_waitcnt vmcnt(2) lgkmcnt(3)
	v_mfma_f32_32x32x16_f16 v[50:65], v[18:21], v[74:77], 0
	v_mfma_f32_32x32x16_f16 v[2:17], v[70:73], v[118:121], v[2:17]
	v_mfma_f32_32x32x16_f16 v[34:49], v[70:73], v[94:97], v[34:49]
	v_lshl_add_u64 v[70:71], s[2:3], 0, v[154:155]
	v_add_co_u32_e32 v152, vcc, s23, v70
	s_nop 1
	v_addc_co_u32_e32 v153, vcc, 0, v71, vcc
	s_waitcnt vmcnt(1) lgkmcnt(2)
	v_mfma_f32_32x32x16_f16 v[50:65], v[22:25], v[78:81], v[50:65]
	v_mfma_f32_32x32x16_f16 v[2:17], v[66:69], v[114:117], v[2:17]
	v_mfma_f32_32x32x16_f16 v[34:49], v[66:69], v[90:93], v[34:49]
	global_load_dwordx4 v[66:69], v154, s[2:3] offset:3072
	s_nop 9
	v_cvt_pk_f16_f32 v9, v8, v9
	v_cvt_pk_f16_f32 v8, v6, v7
	v_cvt_pk_f16_f32 v7, v4, v5
	v_cvt_pk_f16_f32 v6, v2, v3
	v_cvt_pk_f16_f32 v5, v16, v17
	v_cvt_pk_f16_f32 v4, v14, v15
	s_waitcnt vmcnt(1) lgkmcnt(1)
	v_mfma_f32_32x32x16_f16 v[50:65], v[26:29], v[30:33], v[50:65]
	global_load_dwordx4 v[30:33], v168, s[2:3]
	global_load_dwordx4 v[86:89], v[152:153], off offset:1024
	s_nop 0
	global_load_dwordx4 v[168:171], v168, s[0:1]
	v_cvt_pk_f16_f32 v3, v12, v13
	v_cvt_pk_f16_f32 v2, v10, v11
	ds_write_b128 v175, v[6:9]
	ds_write_b128 v174, v[2:5]
	v_cvt_pk_f16_f32 v5, v40, v41
	s_waitcnt vmcnt(3) lgkmcnt(2)
	v_mfma_f32_32x32x16_f16 v[50:65], v[82:85], v[66:69], v[50:65]
	global_load_dwordx4 v[182:185], v154, s[0:1] offset:1024
	v_cvt_pk_f16_f32 v4, v38, v39
	v_cvt_pk_f16_f32 v3, v36, v37
	v_cvt_pk_f16_f32 v2, v34, v35
	ds_write_b128 v175, v[2:5] offset:32768
	v_cvt_pk_f16_f32 v5, v48, v49
	v_cvt_pk_f16_f32 v4, v46, v47
	s_waitcnt vmcnt(3)
	v_mfma_f32_32x32x16_f16 v[66:81], v[18:21], v[30:33], 0
	global_load_dwordx4 v[18:21], v[152:153], off offset:2048
	v_cvt_pk_f16_f32 v3, v44, v45
	v_cvt_pk_f16_f32 v2, v42, v43
	ds_write_b128 v174, v[2:5] offset:32768
	v_cvt_pk_f16_f32 v57, v56, v57
	v_cvt_pk_f16_f32 v56, v54, v55
	v_cvt_pk_f16_f32 v55, v52, v53
	s_waitcnt vmcnt(3)
	v_mfma_f32_32x32x16_f16 v[66:81], v[22:25], v[86:89], v[66:81]
	global_load_dwordx4 v[22:25], v[152:153], off offset:3072
	v_cvt_pk_f16_f32 v54, v50, v51
	s_waitcnt vmcnt(1)
	v_mfma_f32_32x32x16_f16 v[66:81], v[26:29], v[18:21], v[66:81]
	v_lshl_add_u64 v[18:19], s[0:1], 0, v[154:155]
	v_add_co_u32_e32 v152, vcc, s23, v18
	s_nop 1
	v_addc_co_u32_e32 v153, vcc, 0, v19, vcc
	global_load_dwordx4 v[86:89], v[152:153], off offset:1024
	s_waitcnt vmcnt(1)
	v_mfma_f32_32x32x16_f16 v[66:81], v[82:85], v[22:25], v[66:81]
	v_cvt_pk_f16_f32 v85, v64, v65
	v_cvt_pk_f16_f32 v84, v62, v63
	v_cvt_pk_f16_f32 v83, v60, v61
	v_cvt_pk_f16_f32 v82, v58, v59
	v_mfma_f32_32x32x16_f16 v[18:33], v[54:57], v[126:129], 0
	s_nop 6
	v_cvt_pk_f16_f32 v73, v72, v73
	v_cvt_pk_f16_f32 v72, v70, v71
	v_cvt_pk_f16_f32 v70, v66, v67
	v_cvt_pk_f16_f32 v67, v76, v77
	v_cvt_pk_f16_f32 v66, v74, v75
	global_load_dwordx4 v[74:77], v154, s[0:1]
	ds_read_b128 v[2:5], v181
	ds_read_b128 v[6:9], v177
	ds_read_b128 v[10:13], v181 offset:32768
	global_load_dwordx4 v[14:17], v154, s[0:1] offset:2048
	global_load_dwordx4 v[34:37], v154, s[0:1] offset:3072
	v_mfma_f32_32x32x16_f16 v[50:65], v[54:57], v[110:113], 0
	v_cvt_pk_f16_f32 v71, v68, v69
	v_cvt_pk_f16_f32 v69, v80, v81
	v_cvt_pk_f16_f32 v68, v78, v79
	v_mfma_f32_32x32x16_f16 v[18:33], v[82:85], v[122:125], v[18:33]
	v_mfma_f32_32x32x16_f16 v[50:65], v[82:85], v[106:109], v[50:65]
	ds_read_b128 v[82:85], v177 offset:32768
	v_mfma_f32_32x32x16_f16 v[18:33], v[70:73], v[118:121], v[18:33]
	v_mfma_f32_32x32x16_f16 v[50:65], v[70:73], v[94:97], v[50:65]
	v_mfma_f32_32x32x16_f16 v[18:33], v[66:69], v[114:117], v[18:33]
	v_mfma_f32_32x32x16_f16 v[50:65], v[66:69], v[90:93], v[50:65]
	s_nop 10
	v_cvt_pk_f16_f32 v25, v24, v25
	v_cvt_pk_f16_f32 v24, v22, v23
	v_cvt_pk_f16_f32 v23, v20, v21
	v_cvt_pk_f16_f32 v22, v18, v19
	ds_write_b128 v132, v[22:25]
	s_waitcnt vmcnt(2) lgkmcnt(4)
	v_mfma_f32_32x32x16_f16 v[66:81], v[2:5], v[74:77], 0
	s_waitcnt lgkmcnt(3)
	v_mfma_f32_32x32x16_f16 v[66:81], v[6:9], v[182:185], v[66:81]
	s_waitcnt vmcnt(1) lgkmcnt(2)
	v_mfma_f32_32x32x16_f16 v[66:81], v[10:13], v[14:17], v[66:81]
	s_waitcnt vmcnt(0) lgkmcnt(1)
	v_mfma_f32_32x32x16_f16 v[66:81], v[82:85], v[34:37], v[66:81]
	v_mfma_f32_32x32x16_f16 v[34:49], v[2:5], v[168:171], 0
	global_load_dwordx4 v[2:5], v[152:153], off offset:2048
	s_nop 9
	v_cvt_pk_f16_f32 v73, v72, v73
	v_cvt_pk_f16_f32 v72, v70, v71
	v_cvt_pk_f16_f32 v71, v68, v69
	v_cvt_pk_f16_f32 v70, v66, v67
	v_cvt_pk_f16_f32 v69, v80, v81
	v_cvt_pk_f16_f32 v68, v78, v79
	v_mfma_f32_32x32x16_f16 v[34:49], v[6:9], v[86:89], v[34:49]
	global_load_dwordx4 v[6:9], v[152:153], off offset:3072
	v_cvt_pk_f16_f32 v67, v76, v77
	v_cvt_pk_f16_f32 v66, v74, v75
	s_waitcnt vmcnt(1)
	v_mfma_f32_32x32x16_f16 v[34:49], v[10:13], v[2:5], v[34:49]
	s_waitcnt vmcnt(0)
	v_mfma_f32_32x32x16_f16 v[34:49], v[82:85], v[6:9], v[34:49]
	v_mfma_f32_32x32x16_f16 v[2:17], v[70:73], v[126:129], 0
	s_nop 10
	v_cvt_pk_f16_f32 v41, v40, v41
	v_cvt_pk_f16_f32 v40, v38, v39
	v_cvt_pk_f16_f32 v38, v34, v35
	v_cvt_pk_f16_f32 v35, v44, v45
	v_cvt_pk_f16_f32 v34, v42, v43
	v_cvt_pk_f16_f32 v45, v32, v33
	v_cvt_pk_f16_f32 v44, v30, v31
	v_cvt_pk_f16_f32 v43, v28, v29
	v_cvt_pk_f16_f32 v42, v26, v27
	v_mfma_f32_32x32x16_f16 v[18:33], v[70:73], v[110:113], 0
	v_cvt_pk_f16_f32 v39, v36, v37
	v_cvt_pk_f16_f32 v37, v48, v49
	v_cvt_pk_f16_f32 v36, v46, v47
	ds_write_b128 v131, v[42:45]
	v_cvt_pk_f16_f32 v45, v56, v57
	v_cvt_pk_f16_f32 v44, v54, v55
	v_cvt_pk_f16_f32 v43, v52, v53
	v_mfma_f32_32x32x16_f16 v[2:17], v[66:69], v[122:125], v[2:17]
	v_cvt_pk_f16_f32 v42, v50, v51
	ds_write_b128 v132, v[42:45] offset:32768
	v_cvt_pk_f16_f32 v45, v64, v65
	v_cvt_pk_f16_f32 v44, v62, v63
	v_cvt_pk_f16_f32 v43, v60, v61
	v_cvt_pk_f16_f32 v42, v58, v59
	ds_write_b128 v131, v[42:45] offset:32768
	v_mfma_f32_32x32x16_f16 v[18:33], v[66:69], v[106:109], v[18:33]
	v_mfma_f32_32x32x16_f16 v[2:17], v[38:41], v[118:121], v[2:17]
	v_mfma_f32_32x32x16_f16 v[18:33], v[38:41], v[94:97], v[18:33]
	v_mfma_f32_32x32x16_f16 v[2:17], v[34:37], v[114:117], v[2:17]
	v_mfma_f32_32x32x16_f16 v[18:33], v[34:37], v[90:93], v[18:33]
	s_nop 10
	v_cvt_pk_f16_f32 v9, v8, v9
	v_cvt_pk_f16_f32 v8, v6, v7
	v_cvt_pk_f16_f32 v7, v4, v5
	v_cvt_pk_f16_f32 v6, v2, v3
	v_cvt_pk_f16_f32 v5, v16, v17
	v_cvt_pk_f16_f32 v4, v14, v15
	v_cvt_pk_f16_f32 v3, v12, v13
	v_cvt_pk_f16_f32 v2, v10, v11
	ds_write_b128 v135, v[6:9]
	ds_write_b128 v133, v[2:5]
	v_cvt_pk_f16_f32 v5, v24, v25
	v_cvt_pk_f16_f32 v4, v22, v23
	v_cvt_pk_f16_f32 v3, v20, v21
	v_cvt_pk_f16_f32 v2, v18, v19
	ds_write_b128 v135, v[2:5] offset:32768
	v_cvt_pk_f16_f32 v5, v32, v33
	v_cvt_pk_f16_f32 v4, v30, v31
	v_cvt_pk_f16_f32 v3, v28, v29
	v_cvt_pk_f16_f32 v2, v26, v27
	ds_write_b128 v133, v[2:5] offset:32768
	s_setprio 0
	s_waitcnt lgkmcnt(0)
	s_barrier
	s_cmp_lt_i32 s22, 0
	s_cbranch_scc0 .Lno_pref
	s_add_u32 s36, s10, 0x140000
	s_addc_u32 s37, s11, 0
	v_lshlrev_b32_e32 v192, 3, v156
	v_lshlrev_b32_e32 v193, 3, v167
	global_load_dwordx2 v[190:191], v192, s[36:37]
	global_load_dwordx2 v[194:195], v193, s[36:37] offset:2048
